# chunk attention P.V: transposing LDS reads of the next value tile issued before the current tile MFMAs (second register set, counted lgkmcnt)
# speedup vs baseline: 1.0354x; 1.0038x over previous
; #define LAS __attribute__((address_space(3)))
; __device__ __forceinline__ f32x4 mfma16(bf16x8 a, bf16x8 b, f32x4 c) { return __builtin_amdgcn_mfma_f32_16x16x32_bf16(a, b, c, 0, 0, 0); }
; __device__ __forceinline__ void attn_item(const Args& a, int layer, int item, LAS unsigned char* lds) {
;     ...
;         const unsigned kb = cur * 65536 + (2 * hs) * 16384, vb = kb + 16384;
;         f32x4 s[4];
; #pragma unroll
;         for (int kt = 0; kt < 4; ++kt) { f32x4 acc = (f32x4){0.f, 0.f, 0.f, 0.f};
; #pragma unroll
;             for (int ks = 0; ks < 4; ++ks) { const bf16x8 A = *(const LAS bf16x8*)(lds + kb + off_b(16 * kt + fr, 4 * ks + fg)); acc = mfma16(A, Qf[ks].v, acc); }
;             s[kt] = acc; }
;         float mx = -1e30f;
; #pragma unroll
;         for (int kt = 0; kt < 4; ++kt)
; #pragma unroll
;             for (int r = 0; r < 4; ++r) { int rel = qrow + 64 * (8 - jc) - (16 * kt + 4 * fg + r); rel = rel > 256 ? 256 : rel; s[kt][r] = s[kt][r] * scale + Bi[hs * 516 + rel + 256]; mx = fmaxf(mx, s[kt][r]); }
.LBB0_344:
	s_and_b32 s12, s6, 0x10000
	s_add_i32 s13, s12, s7
	v_add_u32_e32 v174, s13, v138
	v_add_u32_e32 v178, v174, v144
	v_add_u32_e32 v186, v174, v145
	ds_read_b128 v[158:161], v178
	ds_read_b128 v[162:165], v178 offset:4096
	ds_read_b128 v[166:169], v186
	ds_read_b128 v[170:173], v186 offset:4096
	s_waitcnt lgkmcnt(3)
	v_mfma_f32_16x16x32_bf16 v[158:161], v[158:161], v[10:13], 0
	v_add_u32_e32 v190, v174, v146
	v_add_u32_e32 v198, v174, v147
	s_add_i32 s13, s13, 0
	s_waitcnt lgkmcnt(1)
	v_mfma_f32_16x16x32_bf16 v[158:161], v[166:169], v[2:5], v[158:161]
	ds_read_b128 v[166:169], v190
	s_addk_i32 s13, 0x4000
	s_andn2_b64 vcc, exec, s[4:5]
	v_mfma_f32_16x16x32_bf16 v[162:165], v[162:165], v[10:13], 0
	s_waitcnt lgkmcnt(1)
	v_mfma_f32_16x16x32_bf16 v[162:165], v[170:173], v[2:5], v[162:165]
	ds_read_b128 v[170:173], v190 offset:4096
	s_waitcnt lgkmcnt(1)
	v_mfma_f32_16x16x32_bf16 v[158:161], v[166:169], v[6:9], v[158:161]
	ds_read_b128 v[166:169], v198
	ds_read_b128 v[174:177], v198 offset:4096
	s_waitcnt lgkmcnt(1)
	v_mfma_f32_16x16x32_bf16 v[158:161], v[166:169], v[14:17], v[158:161]
	ds_read_b128 v[166:169], v178 offset:8192
	ds_read_b128 v[178:181], v178 offset:12288
	ds_read_b128 v[182:185], v186 offset:8192
	ds_read_b128 v[186:189], v186 offset:12288
	s_waitcnt lgkmcnt(3)
	v_mfma_f32_16x16x32_bf16 v[166:169], v[166:169], v[10:13], 0
	v_mfma_f32_16x16x32_bf16 v[162:165], v[170:173], v[6:9], v[162:165]
	ds_read_b128 v[170:173], v190 offset:8192
	ds_read_b128 v[190:193], v190 offset:12288
	ds_read_b128 v[194:197], v198 offset:8192
	ds_read_b128 v[198:201], v198 offset:12288
	s_waitcnt lgkmcnt(5)
	v_mfma_f32_16x16x32_bf16 v[166:169], v[182:185], v[2:5], v[166:169]
	v_mfma_f32_16x16x32_bf16 v[162:165], v[174:177], v[14:17], v[162:165]
	v_add_u32_e32 v174, s11, v156
	v_add_u32_e32 v175, 0x200, v174
	v_add_u32_e32 v176, 0x1ff, v174
	s_waitcnt lgkmcnt(3)
	v_mfma_f32_16x16x32_bf16 v[166:169], v[170:173], v[6:9], v[166:169]
	v_add_u32_e32 v170, 0x1fd, v174
	v_min_i32_e32 v170, 0x100, v170
	v_lshl_add_u32 v182, v170, 2, s8
	v_add_u32_e32 v170, 0x1f0, v174
	v_min_i32_e32 v183, 0x100, v170
	v_mfma_f32_16x16x32_bf16 v[170:173], v[178:181], v[10:13], 0
	v_add_u32_e32 v177, 0x1fe, v174
	v_add_u32_e32 v179, 0x1ef, v174
	v_add_u32_e32 v180, 0x1ee, v174
	v_add_u32_e32 v181, 0x1ed, v174
	v_min_i32_e32 v175, 0x100, v175
	v_min_i32_e32 v176, 0x100, v176
	v_min_i32_e32 v177, 0x100, v177
	v_min_i32_e32 v179, 0x100, v179
	v_min_i32_e32 v180, 0x100, v180
	v_min_i32_e32 v181, 0x100, v181
	v_lshl_add_u32 v175, v175, 2, s8
	v_lshl_add_u32 v176, v176, 2, s8
	v_lshl_add_u32 v177, v177, 2, s8
	v_lshl_add_u32 v178, v183, 2, s8
	v_lshl_add_u32 v179, v179, 2, s8
	v_lshl_add_u32 v180, v180, 2, s8
	v_lshl_add_u32 v181, v181, 2, s8
	v_mfma_f32_16x16x32_bf16 v[170:173], v[186:189], v[2:5], v[170:173]
	ds_read_b32 v175, v175 offset:1024
	ds_read_b32 v176, v176 offset:1024
	ds_read_b32 v177, v177 offset:1024
	ds_read_b32 v182, v182 offset:1024
	ds_read_b32 v178, v178 offset:1024
	ds_read_b32 v179, v179 offset:1024
	ds_read_b32 v180, v180 offset:1024
	ds_read_b32 v181, v181 offset:1024
	s_waitcnt lgkmcnt(6)
	v_fmac_f32_e32 v176, 0x3db504f3, v159
	s_waitcnt lgkmcnt(5)
	v_fmac_f32_e32 v177, 0x3db504f3, v160
	v_mfma_f32_16x16x32_bf16 v[170:173], v[190:193], v[6:9], v[170:173]
	s_waitcnt lgkmcnt(4)
	v_fmac_f32_e32 v182, 0x3db504f3, v161
	s_waitcnt lgkmcnt(3)
	v_fmac_f32_e32 v178, 0x3db504f3, v162
	s_waitcnt lgkmcnt(2)
	v_fmac_f32_e32 v179, 0x3db504f3, v163
	s_waitcnt lgkmcnt(1)
	v_fmac_f32_e32 v180, 0x3db504f3, v164
	s_waitcnt lgkmcnt(0)
	v_fmac_f32_e32 v181, 0x3db504f3, v165
	v_add_u32_e32 v159, 0x1e0, v174
	v_add_u32_e32 v160, 0x1df, v174
	v_add_u32_e32 v161, 0x1de, v174
	v_add_u32_e32 v162, 0x1dd, v174
	v_add_u32_e32 v163, 0x1d0, v174
	v_add_u32_e32 v164, 0x1cf, v174
	v_add_u32_e32 v165, 0x1ce, v174
	v_add_u32_e32 v174, 0x1cd, v174
	v_mfma_f32_16x16x32_bf16 v[166:169], v[194:197], v[14:17], v[166:169]
	v_fmac_f32_e32 v175, 0x3db504f3, v158
	v_min_i32_e32 v159, 0x100, v159
	v_min_i32_e32 v174, 0x100, v174
	v_max3_f32 v158, v175, s77, v176
	v_lshl_add_u32 v159, v159, 2, s8
	v_min_i32_e32 v160, 0x100, v160
	v_min_i32_e32 v161, 0x100, v161
	v_min_i32_e32 v162, 0x100, v162
	v_min_i32_e32 v163, 0x100, v163
	v_min_i32_e32 v164, 0x100, v164
	v_min_i32_e32 v165, 0x100, v165
	v_lshl_add_u32 v174, v174, 2, s8
	v_mfma_f32_16x16x32_bf16 v[170:173], v[198:201], v[14:17], v[170:173]
	v_max3_f32 v158, v158, v177, v182
	v_lshl_add_u32 v160, v160, 2, s8
	v_lshl_add_u32 v161, v161, 2, s8
	v_lshl_add_u32 v162, v162, 2, s8
	v_lshl_add_u32 v163, v163, 2, s8
	v_lshl_add_u32 v164, v164, 2, s8
	v_lshl_add_u32 v165, v165, 2, s8
	ds_read_b32 v183, v159 offset:1024
	ds_read_b32 v184, v160 offset:1024
	ds_read_b32 v185, v161 offset:1024
	ds_read_b32 v186, v162 offset:1024
	ds_read_b32 v187, v163 offset:1024
	ds_read_b32 v188, v164 offset:1024
	ds_read_b32 v189, v165 offset:1024
	ds_read_b32 v174, v174 offset:1024
	v_max3_f32 v158, v158, v178, v179
	v_max3_f32 v158, v158, v180, v181
	s_waitcnt lgkmcnt(7)
	v_fmac_f32_e32 v183, 0x3db504f3, v166
	s_waitcnt lgkmcnt(6)
	v_fmac_f32_e32 v184, 0x3db504f3, v167
	v_max3_f32 v158, v158, v183, v184
	s_waitcnt lgkmcnt(5)
	v_fmac_f32_e32 v185, 0x3db504f3, v168
	s_waitcnt lgkmcnt(4)
	v_fmac_f32_e32 v186, 0x3db504f3, v169
	v_max3_f32 v158, v158, v185, v186
	s_waitcnt lgkmcnt(3)
	v_fmac_f32_e32 v187, 0x3db504f3, v170
	s_waitcnt lgkmcnt(2)
	v_fmac_f32_e32 v188, 0x3db504f3, v171
	v_max3_f32 v158, v158, v187, v188
	s_waitcnt lgkmcnt(1)
	v_fmac_f32_e32 v189, 0x3db504f3, v172
	s_waitcnt lgkmcnt(0)
; __device__ __forceinline__ unsigned pk2(float lo, float hi) { unsigned r; asm volatile("v_cvt_pk_bf16_f32 %0, %1, %2" : "=v"(r) : "v"(lo), "v"(hi)); return r; }
; __device__ __forceinline__ f32x4 mfma16(bf16x8 a, bf16x8 b, f32x4 c) { return __builtin_amdgcn_mfma_f32_16x16x32_bf16(a, b, c, 0, 0, 0); }
; __device__ __forceinline__ void attn_item(const Args& a, int layer, int item, LAS unsigned char* lds) {
;     ...
;         mx = fmaxf(mx, __shfl_xor(mx, 16)); mx = fmaxf(mx, __shfl_xor(mx, 32));
;         const float m_new = fmaxf(m_run, mx), alpha = __expf(m_run - m_new);
;         float ps = 0.f;
; #pragma unroll
;         for (int kt = 0; kt < 4; ++kt)
; #pragma unroll
;             for (int r = 0; r < 4; ++r) { s[kt][r] = __expf(s[kt][r] - m_new); ps += s[kt][r]; }
;         l_run = l_run * alpha + ps; m_run = m_new;
;         FragU Pf[2];
; #pragma unroll
;         for (int k2 = 0; k2 < 2; ++k2) { Pf[k2].u.x = pk2(s[2 * k2][0], s[2 * k2][1]); Pf[k2].u.y = pk2(s[2 * k2][2], s[2 * k2][3]); Pf[k2].u.z = pk2(s[2 * k2 + 1][0], s[2 * k2 + 1][1]); Pf[k2].u.w = pk2(s[2 * k2 + 1][2], s[2 * k2 + 1][3]); }
;         const unsigned q4 = (unsigned)(fr >> 2), p4 = (unsigned)(fr & 3);
; #pragma unroll
;         for (int dt = 0; dt < 8; ++dt) {
;             FragU V0, V1;
;             const unsigned chn = 2 * dt + (p4 >> 1), lo8 = 8 * (p4 & 1);
;             tr_read4(V0.h[0], V0.h[1], V1.h[0], V1.h[1],
;                      ldsb + vb + off_b(4 * fg + q4, chn) + lo8, ldsb + vb + off_b(16 + 4 * fg + q4, chn) + lo8,
;                      ldsb + vb + off_b(32 + 4 * fg + q4, chn) + lo8, ldsb + vb + off_b(48 + 4 * fg + q4, chn) + lo8);
;             f32x4 acc = oacc[dt] * alpha;
;             acc = mfma16(V0.v, Pf[0].v, acc); acc = mfma16(V1.v, Pf[1].v, acc);
;             oacc[dt] = acc; }
	v_fmac_f32_e32 v174, 0x3db504f3, v173
	v_max3_f32 v158, v158, v189, v174
	ds_bpermute_b32 v159, v139, v158
	v_add_u32_e32 v192, s13, v141
	v_add_u32_e32 v193, s13, v142
	v_add_u32_e32 v194, s13, v143
	v_add_u32_e32 v196, v192, v148
	s_waitcnt lgkmcnt(0)
	v_max_f32_e32 v159, v159, v159
	v_max_f32_e32 v158, v158, v159
	ds_bpermute_b32 v159, v137, v158
	v_add_u32_e32 v197, v193, v148
	v_add_u32_e32 v198, v194, v148
	s_waitcnt lgkmcnt(0)
	v_max3_f32 v158, v100, v158, v159
	v_sub_f32_e32 v100, v100, v158
	v_mul_f32_e32 v100, 0x3fb8aa3b, v100
	v_exp_f32_e32 v100, v100
	v_sub_f32_e32 v159, v175, v158
	v_sub_f32_e32 v160, v176, v158
	v_sub_f32_e32 v161, v177, v158
	v_sub_f32_e32 v162, v182, v158
	v_sub_f32_e32 v163, v178, v158
	v_sub_f32_e32 v164, v179, v158
	v_sub_f32_e32 v165, v180, v158
	v_sub_f32_e32 v166, v181, v158
	v_sub_f32_e32 v167, v183, v158
	v_sub_f32_e32 v168, v184, v158
	v_sub_f32_e32 v169, v185, v158
	v_sub_f32_e32 v170, v186, v158
	v_sub_f32_e32 v171, v187, v158
	v_sub_f32_e32 v172, v188, v158
	v_sub_f32_e32 v173, v189, v158
	v_sub_f32_e32 v174, v174, v158
	v_mul_f32_e32 v159, 0x3fb8aa3b, v159
	v_mul_f32_e32 v160, 0x3fb8aa3b, v160
	v_mul_f32_e32 v161, 0x3fb8aa3b, v161
	v_mul_f32_e32 v162, 0x3fb8aa3b, v162
	v_mul_f32_e32 v163, 0x3fb8aa3b, v163
	v_mul_f32_e32 v164, 0x3fb8aa3b, v164
	v_mul_f32_e32 v165, 0x3fb8aa3b, v165
	v_mul_f32_e32 v166, 0x3fb8aa3b, v166
	v_mul_f32_e32 v167, 0x3fb8aa3b, v167
	v_mul_f32_e32 v168, 0x3fb8aa3b, v168
	v_mul_f32_e32 v169, 0x3fb8aa3b, v169
	v_mul_f32_e32 v170, 0x3fb8aa3b, v170
	v_mul_f32_e32 v171, 0x3fb8aa3b, v171
	v_mul_f32_e32 v172, 0x3fb8aa3b, v172
	v_mul_f32_e32 v173, 0x3fb8aa3b, v173
	v_mul_f32_e32 v174, 0x3fb8aa3b, v174
	v_add_u32_e32 v175, s13, v140
	v_pk_mul_f32 v[80:81], v[80:81], v[100:101] op_sel_hi:[1,0]
	v_pk_mul_f32 v[78:79], v[78:79], v[100:101] op_sel_hi:[1,0]
	v_exp_f32_e32 v159, v159
	v_exp_f32_e32 v160, v160
	v_exp_f32_e32 v161, v161
	v_exp_f32_e32 v162, v162
	v_exp_f32_e32 v163, v163
	v_exp_f32_e32 v164, v164
	v_exp_f32_e32 v165, v165
	v_exp_f32_e32 v166, v166
	v_exp_f32_e32 v167, v167
	v_exp_f32_e32 v168, v168
	v_exp_f32_e32 v169, v169
	v_exp_f32_e32 v170, v170
	v_exp_f32_e32 v171, v171
	v_exp_f32_e32 v172, v172
	v_exp_f32_e32 v173, v173
	v_exp_f32_e32 v174, v174
	v_cvt_pk_bf16_f32 v176, v159, v160
	v_cvt_pk_bf16_f32 v177, v161, v162
	v_cvt_pk_bf16_f32 v178, v163, v164
	v_cvt_pk_bf16_f32 v179, v165, v166
	v_cvt_pk_bf16_f32 v180, v167, v168
	v_cvt_pk_bf16_f32 v181, v169, v170
	v_cvt_pk_bf16_f32 v182, v171, v172
	v_cvt_pk_bf16_f32 v183, v173, v174
	v_add_u32_e32 v195, v175, v148
	ds_read_b64_tr_b16 v[188:189], v195
	ds_read_b64_tr_b16 v[190:191], v196
	ds_read_b64_tr_b16 v[184:185], v197
	ds_read_b64_tr_b16 v[186:187], v198
	v_add_u32_e32 v195, v175, v149
	v_add_u32_e32 v196, v192, v149
	v_add_u32_e32 v197, v193, v149
	v_add_u32_e32 v198, v194, v149
	ds_read_b64_tr_b16 v[236:237], v195
	ds_read_b64_tr_b16 v[238:239], v196
	ds_read_b64_tr_b16 v[232:233], v197
	ds_read_b64_tr_b16 v[234:235], v198
	s_waitcnt lgkmcnt(4)
	v_pk_mul_f32 v[76:77], v[76:77], v[100:101] op_sel_hi:[1,0]
	v_mfma_f32_16x16x32_bf16 v[78:81], v[188:191], v[176:179], v[78:81]
	v_mul_f32_e64 v74, v74, v100
	v_mul_f32_e64 v75, v75, v100
	v_mfma_f32_16x16x32_bf16 v[78:81], v[184:187], v[180:183], v[78:81]
	v_add_u32_e32 v195, v175, v150
	v_add_u32_e32 v196, v192, v150
	v_add_u32_e32 v197, v193, v150
	v_add_u32_e32 v198, v194, v150
	ds_read_b64_tr_b16 v[188:189], v195
	ds_read_b64_tr_b16 v[190:191], v196
	ds_read_b64_tr_b16 v[184:185], v197
	ds_read_b64_tr_b16 v[186:187], v198
	s_waitcnt lgkmcnt(4)
	v_pk_mul_f32 v[72:73], v[72:73], v[100:101] op_sel_hi:[1,0]
	v_mfma_f32_16x16x32_bf16 v[74:77], v[236:239], v[176:179], v[74:77]
	v_mul_f32_e64 v70, v70, v100
	v_mul_f32_e64 v71, v71, v100
	v_mfma_f32_16x16x32_bf16 v[74:77], v[232:235], v[180:183], v[74:77]
	v_add_u32_e32 v195, v175, v151
	v_add_u32_e32 v196, v192, v151
	v_add_u32_e32 v197, v193, v151
	v_add_u32_e32 v198, v194, v151
	ds_read_b64_tr_b16 v[236:237], v195
	ds_read_b64_tr_b16 v[238:239], v196
	ds_read_b64_tr_b16 v[232:233], v197
	ds_read_b64_tr_b16 v[234:235], v198
	s_waitcnt lgkmcnt(4)
	v_pk_mul_f32 v[68:69], v[68:69], v[100:101] op_sel_hi:[1,0]
	v_mfma_f32_16x16x32_bf16 v[70:73], v[188:191], v[176:179], v[70:73]
	v_mul_f32_e64 v66, v66, v100
	v_mul_f32_e64 v67, v67, v100
	v_mfma_f32_16x16x32_bf16 v[70:73], v[184:187], v[180:183], v[70:73]
	v_add_u32_e32 v195, v175, v152
	v_add_u32_e32 v196, v192, v152
	v_add_u32_e32 v197, v193, v152
	v_add_u32_e32 v198, v194, v152
	ds_read_b64_tr_b16 v[188:189], v195
	ds_read_b64_tr_b16 v[190:191], v196
	ds_read_b64_tr_b16 v[184:185], v197
	ds_read_b64_tr_b16 v[186:187], v198
	s_waitcnt lgkmcnt(4)
	v_pk_mul_f32 v[64:65], v[64:65], v[100:101] op_sel_hi:[1,0]
	v_mfma_f32_16x16x32_bf16 v[66:69], v[236:239], v[176:179], v[66:69]
	v_mul_f32_e64 v62, v62, v100
	v_mul_f32_e64 v63, v63, v100
	v_mfma_f32_16x16x32_bf16 v[66:69], v[232:235], v[180:183], v[66:69]
	v_add_u32_e32 v195, v175, v153
	v_add_u32_e32 v196, v192, v153
	v_add_u32_e32 v197, v193, v153
	v_add_u32_e32 v198, v194, v153
	ds_read_b64_tr_b16 v[236:237], v195
	ds_read_b64_tr_b16 v[238:239], v196
	ds_read_b64_tr_b16 v[232:233], v197
	ds_read_b64_tr_b16 v[234:235], v198
	s_waitcnt lgkmcnt(4)
	v_pk_mul_f32 v[60:61], v[60:61], v[100:101] op_sel_hi:[1,0]
	v_mfma_f32_16x16x32_bf16 v[62:65], v[188:191], v[176:179], v[62:65]
	v_mul_f32_e64 v58, v58, v100
	v_mul_f32_e64 v59, v59, v100
	v_mfma_f32_16x16x32_bf16 v[62:65], v[184:187], v[180:183], v[62:65]
	v_add_u32_e32 v195, v175, v154
	v_add_u32_e32 v196, v192, v154
	v_add_u32_e32 v197, v193, v154
	v_add_u32_e32 v198, v194, v154
	ds_read_b64_tr_b16 v[188:189], v195
	ds_read_b64_tr_b16 v[190:191], v196
	ds_read_b64_tr_b16 v[184:185], v197
	ds_read_b64_tr_b16 v[186:187], v198
	s_waitcnt lgkmcnt(4)
	v_pk_mul_f32 v[56:57], v[56:57], v[100:101] op_sel_hi:[1,0]
	v_mfma_f32_16x16x32_bf16 v[58:61], v[236:239], v[176:179], v[58:61]
	v_mul_f32_e64 v54, v54, v100
	v_mul_f32_e64 v55, v55, v100
	v_mfma_f32_16x16x32_bf16 v[58:61], v[232:235], v[180:183], v[58:61]
	v_add_u32_e32 v175, v175, v155
	v_add_u32_e32 v192, v192, v155
	v_add_u32_e32 v193, v193, v155
	v_add_u32_e32 v194, v194, v155
	ds_read_b64_tr_b16 v[236:237], v175
	ds_read_b64_tr_b16 v[238:239], v192
	ds_read_b64_tr_b16 v[232:233], v193
	ds_read_b64_tr_b16 v[234:235], v194
	s_waitcnt lgkmcnt(4)
	v_pk_mul_f32 v[52:53], v[52:53], v[100:101] op_sel_hi:[1,0]
	v_mfma_f32_16x16x32_bf16 v[54:57], v[188:191], v[176:179], v[54:57]
	v_mul_f32_e64 v50, v50, v100
	v_mul_f32_e64 v51, v51, v100
	v_mfma_f32_16x16x32_bf16 v[54:57], v[184:187], v[180:183], v[54:57]
	s_waitcnt lgkmcnt(0)
	s_nop 0
	v_mfma_f32_16x16x32_bf16 v[50:53], v[236:239], v[176:179], v[50:53]
	v_mfma_f32_16x16x32_bf16 v[50:53], v[232:235], v[180:183], v[50:53]
	s_cbranch_vccnz .LBB0_346
; #define LAS __attribute__((address_space(3)))
; __device__ __forceinline__ void attn_item(const Args& a, int layer, int item, LAS unsigned char* lds) {
;     ...
;         if (jc < 8) {
; #pragma unroll
;             for (int i = 0; i < 8; ++i) { const int c = tid + i * NTHR, tile = c >> 10, row = (c >> 4) & 63, ch = c & 15; *(LAS u32x4*)(lds + (cur ^ 1) * 65536 + tile * 16384 + off_b(row, ch)) = st[i]; } }
	s_xor_b32 s4, s12, 0x10000
	s_add_i32 s4, s4, 0
	v_add_u32_e32 v175, s4, v112
	v_add3_u32 v175, v175, v114, v113
	s_waitcnt vmcnt(7)
	ds_write_b128 v175, v[18:21]
	v_add_u32_e32 v175, s4, v115
	v_add3_u32 v175, v175, v117, v116
	s_waitcnt vmcnt(6)
	ds_write_b128 v175, v[22:25]
	v_add_u32_e32 v175, s4, v118
	v_add3_u32 v175, v175, v120, v119
	s_waitcnt vmcnt(5)
	ds_write_b128 v175, v[26:29]
	v_add_u32_e32 v175, s4, v121
	v_add3_u32 v175, v175, v123, v122
	s_waitcnt vmcnt(4)
	ds_write_b128 v175, v[30:33]
	v_add_u32_e32 v175, s4, v124
	v_add3_u32 v175, v175, v126, v125
	s_waitcnt vmcnt(3)
	ds_write_b128 v175, v[34:37]
	v_add_u32_e32 v175, s4, v127
	v_add3_u32 v175, v175, v129, v128
	s_waitcnt vmcnt(2)
	ds_write_b128 v175, v[38:41]
	v_add_u32_e32 v175, s4, v130
	v_add3_u32 v175, v175, v132, v131
	s_waitcnt vmcnt(1)
	ds_write_b128 v175, v[42:45]
	v_add_u32_e32 v175, s4, v133
	v_add3_u32 v175, v175, v135, v134
	s_waitcnt vmcnt(0)
	ds_write_b128 v175, v[46:49]

; #define LAS __attribute__((address_space(3)))
; __device__ __forceinline__ f32x4 mfma16(bf16x8 a, bf16x8 b, f32x4 c) { return __builtin_amdgcn_mfma_f32_16x16x32_bf16(a, b, c, 0, 0, 0); }
; __device__ __forceinline__ void attn_item(const Args& a, int layer, int item, LAS unsigned char* lds) {
;     ...
;         const unsigned kb = cur * 65536 + (2 * hs) * 16384, vb = kb + 16384;
;         f32x4 s[4];
; #pragma unroll
;         for (int kt = 0; kt < 4; ++kt) { f32x4 acc = (f32x4){0.f, 0.f, 0.f, 0.f};
; #pragma unroll
;             for (int ks = 0; ks < 4; ++ks) { const bf16x8 A = *(const LAS bf16x8*)(lds + kb + off_b(16 * kt + fr, 4 * ks + fg)); acc = mfma16(A, Qf[ks].v, acc); }
;             s[kt] = acc; }
;         float mx = -1e30f;
; #pragma unroll
;         for (int kt = 0; kt < 4; ++kt)
; #pragma unroll
;             for (int r = 0; r < 4; ++r) { int rel = qrow + 64 * (8 - jc) - (16 * kt + 4 * fg + r); rel = rel > 256 ? 256 : rel; s[kt][r] = s[kt][r] * scale + Bi[hs * 516 + rel + 256]; mx = fmaxf(mx, s[kt][r]); }
.LBB0_1411:
	s_and_b32 s51, s50, 0x10000
	s_add_i32 s52, s51, s48
	v_add_u32_e32 v174, s52, v138
	v_add_u32_e32 v178, v174, v144
	v_add_u32_e32 v186, v174, v145
	ds_read_b128 v[158:161], v178
	ds_read_b128 v[162:165], v178 offset:4096
	ds_read_b128 v[166:169], v186
	ds_read_b128 v[170:173], v186 offset:4096
	s_waitcnt lgkmcnt(3)
	v_mfma_f32_16x16x32_bf16 v[158:161], v[158:161], v[10:13], 0
	v_add_u32_e32 v190, v174, v146
	v_add_u32_e32 v198, v174, v147
	s_add_i32 s34, s52, 0
	s_waitcnt lgkmcnt(1)
	v_mfma_f32_16x16x32_bf16 v[158:161], v[166:169], v[2:5], v[158:161]
	ds_read_b128 v[166:169], v190
	s_addk_i32 s34, 0x4000
	s_andn2_b64 vcc, exec, s[4:5]
	v_mfma_f32_16x16x32_bf16 v[162:165], v[162:165], v[10:13], 0
	s_waitcnt lgkmcnt(1)
	v_mfma_f32_16x16x32_bf16 v[162:165], v[170:173], v[2:5], v[162:165]
	ds_read_b128 v[170:173], v190 offset:4096
	s_waitcnt lgkmcnt(1)
	v_mfma_f32_16x16x32_bf16 v[158:161], v[166:169], v[6:9], v[158:161]
	ds_read_b128 v[166:169], v198
	ds_read_b128 v[174:177], v198 offset:4096
	s_waitcnt lgkmcnt(1)
	v_mfma_f32_16x16x32_bf16 v[158:161], v[166:169], v[14:17], v[158:161]
	ds_read_b128 v[166:169], v178 offset:8192
	ds_read_b128 v[178:181], v178 offset:12288
	ds_read_b128 v[182:185], v186 offset:8192
	ds_read_b128 v[186:189], v186 offset:12288
	s_waitcnt lgkmcnt(3)
	v_mfma_f32_16x16x32_bf16 v[166:169], v[166:169], v[10:13], 0
	v_mfma_f32_16x16x32_bf16 v[162:165], v[170:173], v[6:9], v[162:165]
	ds_read_b128 v[170:173], v190 offset:8192
	ds_read_b128 v[190:193], v190 offset:12288
	ds_read_b128 v[194:197], v198 offset:8192
	ds_read_b128 v[198:201], v198 offset:12288
	s_waitcnt lgkmcnt(5)
	v_mfma_f32_16x16x32_bf16 v[166:169], v[182:185], v[2:5], v[166:169]
	v_mfma_f32_16x16x32_bf16 v[162:165], v[174:177], v[14:17], v[162:165]
	v_add_u32_e32 v174, s47, v156
	v_add_u32_e32 v175, 0x200, v174
	v_add_u32_e32 v176, 0x1ff, v174
	s_waitcnt lgkmcnt(3)
	v_mfma_f32_16x16x32_bf16 v[166:169], v[170:173], v[6:9], v[166:169]
	v_add_u32_e32 v170, 0x1fd, v174
	v_min_i32_e32 v170, 0x100, v170
	v_lshl_add_u32 v182, v170, 2, s49
	v_add_u32_e32 v170, 0x1f0, v174
	v_min_i32_e32 v183, 0x100, v170
	v_mfma_f32_16x16x32_bf16 v[170:173], v[178:181], v[10:13], 0
	v_add_u32_e32 v177, 0x1fe, v174
	v_add_u32_e32 v179, 0x1ef, v174
	v_add_u32_e32 v180, 0x1ee, v174
	v_add_u32_e32 v181, 0x1ed, v174
	v_min_i32_e32 v175, 0x100, v175
	v_min_i32_e32 v176, 0x100, v176
	v_min_i32_e32 v177, 0x100, v177
	v_min_i32_e32 v179, 0x100, v179
	v_min_i32_e32 v180, 0x100, v180
	v_min_i32_e32 v181, 0x100, v181
	v_lshl_add_u32 v175, v175, 2, s49
	v_lshl_add_u32 v176, v176, 2, s49
	v_lshl_add_u32 v177, v177, 2, s49
	v_lshl_add_u32 v178, v183, 2, s49
	v_lshl_add_u32 v179, v179, 2, s49
	v_lshl_add_u32 v180, v180, 2, s49
	v_lshl_add_u32 v181, v181, 2, s49
	v_mfma_f32_16x16x32_bf16 v[170:173], v[186:189], v[2:5], v[170:173]
	ds_read_b32 v175, v175 offset:1024
	ds_read_b32 v176, v176 offset:1024
	ds_read_b32 v177, v177 offset:1024
	ds_read_b32 v182, v182 offset:1024
	ds_read_b32 v178, v178 offset:1024
	ds_read_b32 v179, v179 offset:1024
	ds_read_b32 v180, v180 offset:1024
	ds_read_b32 v181, v181 offset:1024
	s_waitcnt lgkmcnt(6)
	v_fmac_f32_e32 v176, 0x3db504f3, v159
	s_waitcnt lgkmcnt(5)
	v_fmac_f32_e32 v177, 0x3db504f3, v160
	v_mfma_f32_16x16x32_bf16 v[170:173], v[190:193], v[6:9], v[170:173]
	s_waitcnt lgkmcnt(4)
	v_fmac_f32_e32 v182, 0x3db504f3, v161
	s_waitcnt lgkmcnt(3)
	v_fmac_f32_e32 v178, 0x3db504f3, v162
	s_waitcnt lgkmcnt(2)
	v_fmac_f32_e32 v179, 0x3db504f3, v163
	s_waitcnt lgkmcnt(1)
	v_fmac_f32_e32 v180, 0x3db504f3, v164
	s_waitcnt lgkmcnt(0)
	v_fmac_f32_e32 v181, 0x3db504f3, v165
	v_add_u32_e32 v159, 0x1e0, v174
	v_add_u32_e32 v160, 0x1df, v174
	v_add_u32_e32 v161, 0x1de, v174
	v_add_u32_e32 v162, 0x1dd, v174
	v_add_u32_e32 v163, 0x1d0, v174
	v_add_u32_e32 v164, 0x1cf, v174
	v_add_u32_e32 v165, 0x1ce, v174
	v_add_u32_e32 v174, 0x1cd, v174
	v_mfma_f32_16x16x32_bf16 v[166:169], v[194:197], v[14:17], v[166:169]
	v_fmac_f32_e32 v175, 0x3db504f3, v158
	v_min_i32_e32 v159, 0x100, v159
	v_min_i32_e32 v174, 0x100, v174
	v_max3_f32 v158, v175, s87, v176
	v_lshl_add_u32 v159, v159, 2, s49
	v_min_i32_e32 v160, 0x100, v160
	v_min_i32_e32 v161, 0x100, v161
	v_min_i32_e32 v162, 0x100, v162
	v_min_i32_e32 v163, 0x100, v163
	v_min_i32_e32 v164, 0x100, v164
	v_min_i32_e32 v165, 0x100, v165
	v_lshl_add_u32 v174, v174, 2, s49
	v_mfma_f32_16x16x32_bf16 v[170:173], v[198:201], v[14:17], v[170:173]
	v_max3_f32 v158, v158, v177, v182
	v_lshl_add_u32 v160, v160, 2, s49
	v_lshl_add_u32 v161, v161, 2, s49
	v_lshl_add_u32 v162, v162, 2, s49
	v_lshl_add_u32 v163, v163, 2, s49
	v_lshl_add_u32 v164, v164, 2, s49
	v_lshl_add_u32 v165, v165, 2, s49
	ds_read_b32 v183, v159 offset:1024
	ds_read_b32 v184, v160 offset:1024
	ds_read_b32 v185, v161 offset:1024
	ds_read_b32 v186, v162 offset:1024
	ds_read_b32 v187, v163 offset:1024
	ds_read_b32 v188, v164 offset:1024
	ds_read_b32 v189, v165 offset:1024
	ds_read_b32 v174, v174 offset:1024
	v_max3_f32 v158, v158, v178, v179
	v_max3_f32 v158, v158, v180, v181
	s_waitcnt lgkmcnt(7)
	v_fmac_f32_e32 v183, 0x3db504f3, v166
	s_waitcnt lgkmcnt(6)
	v_fmac_f32_e32 v184, 0x3db504f3, v167
	v_max3_f32 v158, v158, v183, v184
	s_waitcnt lgkmcnt(5)
	v_fmac_f32_e32 v185, 0x3db504f3, v168
	s_waitcnt lgkmcnt(4)
	v_fmac_f32_e32 v186, 0x3db504f3, v169
	v_max3_f32 v158, v158, v185, v186
	s_waitcnt lgkmcnt(3)
	v_fmac_f32_e32 v187, 0x3db504f3, v170
	s_waitcnt lgkmcnt(2)
	v_fmac_f32_e32 v188, 0x3db504f3, v171
	v_max3_f32 v158, v158, v187, v188
	s_waitcnt lgkmcnt(1)
	v_fmac_f32_e32 v189, 0x3db504f3, v172
	s_waitcnt lgkmcnt(0)
; __device__ __forceinline__ unsigned pk2(float lo, float hi) { unsigned r; asm volatile("v_cvt_pk_bf16_f32 %0, %1, %2" : "=v"(r) : "v"(lo), "v"(hi)); return r; }
; __device__ __forceinline__ f32x4 mfma16(bf16x8 a, bf16x8 b, f32x4 c) { return __builtin_amdgcn_mfma_f32_16x16x32_bf16(a, b, c, 0, 0, 0); }
; __device__ __forceinline__ void attn_item(const Args& a, int layer, int item, LAS unsigned char* lds) {
;     ...
;         mx = fmaxf(mx, __shfl_xor(mx, 16)); mx = fmaxf(mx, __shfl_xor(mx, 32));
;         const float m_new = fmaxf(m_run, mx), alpha = __expf(m_run - m_new);
;         float ps = 0.f;
; #pragma unroll
;         for (int kt = 0; kt < 4; ++kt)
; #pragma unroll
;             for (int r = 0; r < 4; ++r) { s[kt][r] = __expf(s[kt][r] - m_new); ps += s[kt][r]; }
;         l_run = l_run * alpha + ps; m_run = m_new;
;         FragU Pf[2];
; #pragma unroll
;         for (int k2 = 0; k2 < 2; ++k2) { Pf[k2].u.x = pk2(s[2 * k2][0], s[2 * k2][1]); Pf[k2].u.y = pk2(s[2 * k2][2], s[2 * k2][3]); Pf[k2].u.z = pk2(s[2 * k2 + 1][0], s[2 * k2 + 1][1]); Pf[k2].u.w = pk2(s[2 * k2 + 1][2], s[2 * k2 + 1][3]); }
;         const unsigned q4 = (unsigned)(fr >> 2), p4 = (unsigned)(fr & 3);
; #pragma unroll
;         for (int dt = 0; dt < 8; ++dt) {
;             FragU V0, V1;
;             const unsigned chn = 2 * dt + (p4 >> 1), lo8 = 8 * (p4 & 1);
;             tr_read4(V0.h[0], V0.h[1], V1.h[0], V1.h[1],
;                      ldsb + vb + off_b(4 * fg + q4, chn) + lo8, ldsb + vb + off_b(16 + 4 * fg + q4, chn) + lo8,
;                      ldsb + vb + off_b(32 + 4 * fg + q4, chn) + lo8, ldsb + vb + off_b(48 + 4 * fg + q4, chn) + lo8);
;             f32x4 acc = oacc[dt] * alpha;
;             acc = mfma16(V0.v, Pf[0].v, acc); acc = mfma16(V1.v, Pf[1].v, acc);
;             oacc[dt] = acc; }
	v_fmac_f32_e32 v174, 0x3db504f3, v173
	v_max3_f32 v158, v158, v189, v174
	ds_bpermute_b32 v159, v139, v158
	v_add_u32_e32 v192, s34, v141
	v_add_u32_e32 v193, s34, v142
	v_add_u32_e32 v194, s34, v143
	v_add_u32_e32 v196, v192, v148
	s_waitcnt lgkmcnt(0)
	v_max_f32_e32 v159, v159, v159
	v_max_f32_e32 v158, v158, v159
	ds_bpermute_b32 v159, v137, v158
	v_add_u32_e32 v197, v193, v148
	v_add_u32_e32 v198, v194, v148
	s_waitcnt lgkmcnt(0)
	v_max3_f32 v158, v100, v158, v159
	v_sub_f32_e32 v100, v100, v158
	v_mul_f32_e32 v100, 0x3fb8aa3b, v100
	v_exp_f32_e32 v100, v100
	v_sub_f32_e32 v159, v175, v158
	v_sub_f32_e32 v160, v176, v158
	v_sub_f32_e32 v161, v177, v158
	v_sub_f32_e32 v162, v182, v158
	v_sub_f32_e32 v163, v178, v158
	v_sub_f32_e32 v164, v179, v158
	v_sub_f32_e32 v165, v180, v158
	v_sub_f32_e32 v166, v181, v158
	v_sub_f32_e32 v167, v183, v158
	v_sub_f32_e32 v168, v184, v158
	v_sub_f32_e32 v169, v185, v158
	v_sub_f32_e32 v170, v186, v158
	v_sub_f32_e32 v171, v187, v158
	v_sub_f32_e32 v172, v188, v158
	v_sub_f32_e32 v173, v189, v158
	v_sub_f32_e32 v174, v174, v158
	v_mul_f32_e32 v159, 0x3fb8aa3b, v159
	v_mul_f32_e32 v160, 0x3fb8aa3b, v160
	v_mul_f32_e32 v161, 0x3fb8aa3b, v161
	v_mul_f32_e32 v162, 0x3fb8aa3b, v162
	v_mul_f32_e32 v163, 0x3fb8aa3b, v163
	v_mul_f32_e32 v164, 0x3fb8aa3b, v164
	v_mul_f32_e32 v165, 0x3fb8aa3b, v165
	v_mul_f32_e32 v166, 0x3fb8aa3b, v166
	v_mul_f32_e32 v167, 0x3fb8aa3b, v167
	v_mul_f32_e32 v168, 0x3fb8aa3b, v168
	v_mul_f32_e32 v169, 0x3fb8aa3b, v169
	v_mul_f32_e32 v170, 0x3fb8aa3b, v170
	v_mul_f32_e32 v171, 0x3fb8aa3b, v171
	v_mul_f32_e32 v172, 0x3fb8aa3b, v172
	v_mul_f32_e32 v173, 0x3fb8aa3b, v173
	v_mul_f32_e32 v174, 0x3fb8aa3b, v174
	v_add_u32_e32 v175, s34, v140
	v_pk_mul_f32 v[80:81], v[80:81], v[100:101] op_sel_hi:[1,0]
	v_pk_mul_f32 v[78:79], v[78:79], v[100:101] op_sel_hi:[1,0]
	v_exp_f32_e32 v159, v159
	v_exp_f32_e32 v160, v160
	v_exp_f32_e32 v161, v161
	v_exp_f32_e32 v162, v162
	v_exp_f32_e32 v163, v163
	v_exp_f32_e32 v164, v164
	v_exp_f32_e32 v165, v165
	v_exp_f32_e32 v166, v166
	v_exp_f32_e32 v167, v167
	v_exp_f32_e32 v168, v168
	v_exp_f32_e32 v169, v169
	v_exp_f32_e32 v170, v170
	v_exp_f32_e32 v171, v171
	v_exp_f32_e32 v172, v172
	v_exp_f32_e32 v173, v173
	v_exp_f32_e32 v174, v174
	v_cvt_pk_bf16_f32 v176, v159, v160
	v_cvt_pk_bf16_f32 v177, v161, v162
	v_cvt_pk_bf16_f32 v178, v163, v164
	v_cvt_pk_bf16_f32 v179, v165, v166
	v_cvt_pk_bf16_f32 v180, v167, v168
	v_cvt_pk_bf16_f32 v181, v169, v170
	v_cvt_pk_bf16_f32 v182, v171, v172
	v_cvt_pk_bf16_f32 v183, v173, v174
	v_add_u32_e32 v195, v175, v148
	ds_read_b64_tr_b16 v[188:189], v195
	ds_read_b64_tr_b16 v[190:191], v196
	ds_read_b64_tr_b16 v[184:185], v197
	ds_read_b64_tr_b16 v[186:187], v198
	v_add_u32_e32 v195, v175, v149
	v_add_u32_e32 v196, v192, v149
	v_add_u32_e32 v197, v193, v149
	v_add_u32_e32 v198, v194, v149
	ds_read_b64_tr_b16 v[236:237], v195
	ds_read_b64_tr_b16 v[238:239], v196
	ds_read_b64_tr_b16 v[232:233], v197
	ds_read_b64_tr_b16 v[234:235], v198
	s_waitcnt lgkmcnt(4)
	v_pk_mul_f32 v[76:77], v[76:77], v[100:101] op_sel_hi:[1,0]
	v_mfma_f32_16x16x32_bf16 v[78:81], v[188:191], v[176:179], v[78:81]
	v_mul_f32_e64 v74, v74, v100
	v_mul_f32_e64 v75, v75, v100
	v_mfma_f32_16x16x32_bf16 v[78:81], v[184:187], v[180:183], v[78:81]
	v_add_u32_e32 v195, v175, v150
	v_add_u32_e32 v196, v192, v150
	v_add_u32_e32 v197, v193, v150
	v_add_u32_e32 v198, v194, v150
	ds_read_b64_tr_b16 v[188:189], v195
	ds_read_b64_tr_b16 v[190:191], v196
	ds_read_b64_tr_b16 v[184:185], v197
	ds_read_b64_tr_b16 v[186:187], v198
	s_waitcnt lgkmcnt(4)
	v_pk_mul_f32 v[72:73], v[72:73], v[100:101] op_sel_hi:[1,0]
	v_mfma_f32_16x16x32_bf16 v[74:77], v[236:239], v[176:179], v[74:77]
	v_mul_f32_e64 v70, v70, v100
	v_mul_f32_e64 v71, v71, v100
	v_mfma_f32_16x16x32_bf16 v[74:77], v[232:235], v[180:183], v[74:77]
	v_add_u32_e32 v195, v175, v151
	v_add_u32_e32 v196, v192, v151
	v_add_u32_e32 v197, v193, v151
	v_add_u32_e32 v198, v194, v151
	ds_read_b64_tr_b16 v[236:237], v195
	ds_read_b64_tr_b16 v[238:239], v196
	ds_read_b64_tr_b16 v[232:233], v197
	ds_read_b64_tr_b16 v[234:235], v198
	s_waitcnt lgkmcnt(4)
	v_pk_mul_f32 v[68:69], v[68:69], v[100:101] op_sel_hi:[1,0]
	v_mfma_f32_16x16x32_bf16 v[70:73], v[188:191], v[176:179], v[70:73]
	v_mul_f32_e64 v66, v66, v100
	v_mul_f32_e64 v67, v67, v100
	v_mfma_f32_16x16x32_bf16 v[70:73], v[184:187], v[180:183], v[70:73]
	v_add_u32_e32 v195, v175, v152
	v_add_u32_e32 v196, v192, v152
	v_add_u32_e32 v197, v193, v152
	v_add_u32_e32 v198, v194, v152
	ds_read_b64_tr_b16 v[188:189], v195
	ds_read_b64_tr_b16 v[190:191], v196
	ds_read_b64_tr_b16 v[184:185], v197
	ds_read_b64_tr_b16 v[186:187], v198
	s_waitcnt lgkmcnt(4)
	v_pk_mul_f32 v[64:65], v[64:65], v[100:101] op_sel_hi:[1,0]
	v_mfma_f32_16x16x32_bf16 v[66:69], v[236:239], v[176:179], v[66:69]
	v_mul_f32_e64 v62, v62, v100
	v_mul_f32_e64 v63, v63, v100
	v_mfma_f32_16x16x32_bf16 v[66:69], v[232:235], v[180:183], v[66:69]
	v_add_u32_e32 v195, v175, v153
	v_add_u32_e32 v196, v192, v153
	v_add_u32_e32 v197, v193, v153
	v_add_u32_e32 v198, v194, v153
	ds_read_b64_tr_b16 v[236:237], v195
	ds_read_b64_tr_b16 v[238:239], v196
	ds_read_b64_tr_b16 v[232:233], v197
	ds_read_b64_tr_b16 v[234:235], v198
	s_waitcnt lgkmcnt(4)
	v_pk_mul_f32 v[60:61], v[60:61], v[100:101] op_sel_hi:[1,0]
	v_mfma_f32_16x16x32_bf16 v[62:65], v[188:191], v[176:179], v[62:65]
	v_mul_f32_e64 v58, v58, v100
	v_mul_f32_e64 v59, v59, v100
	v_mfma_f32_16x16x32_bf16 v[62:65], v[184:187], v[180:183], v[62:65]
	v_add_u32_e32 v195, v175, v154
	v_add_u32_e32 v196, v192, v154
	v_add_u32_e32 v197, v193, v154
	v_add_u32_e32 v198, v194, v154
	ds_read_b64_tr_b16 v[188:189], v195
	ds_read_b64_tr_b16 v[190:191], v196
	ds_read_b64_tr_b16 v[184:185], v197
	ds_read_b64_tr_b16 v[186:187], v198
	s_waitcnt lgkmcnt(4)
	v_pk_mul_f32 v[56:57], v[56:57], v[100:101] op_sel_hi:[1,0]
	v_mfma_f32_16x16x32_bf16 v[58:61], v[236:239], v[176:179], v[58:61]
	v_mul_f32_e64 v54, v54, v100
	v_mul_f32_e64 v55, v55, v100
	v_mfma_f32_16x16x32_bf16 v[58:61], v[232:235], v[180:183], v[58:61]
	v_add_u32_e32 v175, v175, v155
	v_add_u32_e32 v192, v192, v155
	v_add_u32_e32 v193, v193, v155
	v_add_u32_e32 v194, v194, v155
	ds_read_b64_tr_b16 v[236:237], v175
	ds_read_b64_tr_b16 v[238:239], v192
	ds_read_b64_tr_b16 v[232:233], v193
	ds_read_b64_tr_b16 v[234:235], v194
	s_waitcnt lgkmcnt(4)
	v_pk_mul_f32 v[52:53], v[52:53], v[100:101] op_sel_hi:[1,0]
	v_mfma_f32_16x16x32_bf16 v[54:57], v[188:191], v[176:179], v[54:57]
	v_mul_f32_e64 v50, v50, v100
	v_mul_f32_e64 v51, v51, v100
	v_mfma_f32_16x16x32_bf16 v[54:57], v[184:187], v[180:183], v[54:57]
	s_waitcnt lgkmcnt(0)
	s_nop 0
	v_mfma_f32_16x16x32_bf16 v[50:53], v[236:239], v[176:179], v[50:53]
	v_mfma_f32_16x16x32_bf16 v[50:53], v[232:235], v[180:183], v[50:53]
	s_cbranch_vccnz .LBB0_1413
; #define LAS __attribute__((address_space(3)))
; __device__ __forceinline__ void attn_item(const Args& a, int layer, int item, LAS unsigned char* lds) {
;     ...
;         if (jc < 8) {
; #pragma unroll
;             for (int i = 0; i < 8; ++i) { const int c = tid + i * NTHR, tile = c >> 10, row = (c >> 4) & 63, ch = c & 15; *(LAS u32x4*)(lds + (cur ^ 1) * 65536 + tile * 16384 + off_b(row, ch)) = st[i]; } }
	s_xor_b32 s4, s51, 0x10000
	s_add_i32 s4, s4, 0
	v_add_u32_e32 v175, s4, v112
	v_add3_u32 v175, v175, v114, v113
	s_waitcnt vmcnt(7)
	ds_write_b128 v175, v[18:21]
	v_add_u32_e32 v175, s4, v115
	v_add3_u32 v175, v175, v117, v116
	s_waitcnt vmcnt(6)
	ds_write_b128 v175, v[22:25]
	v_add_u32_e32 v175, s4, v118
	v_add3_u32 v175, v175, v120, v119
	s_waitcnt vmcnt(5)
	ds_write_b128 v175, v[26:29]
	v_add_u32_e32 v175, s4, v121
	v_add3_u32 v175, v175, v123, v122
	s_waitcnt vmcnt(4)
	ds_write_b128 v175, v[30:33]
	v_add_u32_e32 v175, s4, v124
	v_add3_u32 v175, v175, v126, v125
	s_waitcnt vmcnt(3)
	ds_write_b128 v175, v[34:37]
	v_add_u32_e32 v175, s4, v127
	v_add3_u32 v175, v175, v129, v128
	s_waitcnt vmcnt(2)
	ds_write_b128 v175, v[38:41]
	v_add_u32_e32 v175, s4, v130
	v_add3_u32 v175, v175, v132, v131
	s_waitcnt vmcnt(1)
	ds_write_b128 v175, v[42:45]
	v_add_u32_e32 v175, s4, v133
	v_add3_u32 v175, v175, v135, v134
	s_waitcnt vmcnt(0)
	ds_write_b128 v175, v[46:49]
